# P1 conv tiles 10032->9576 (6 fewer per converter WG), P7 tail 1360->1816
# speedup vs baseline: 1.0051x; 1.0050x over previous
.LBB0_86:
	s_cmp_lt_i32 s50, 2
	s_cselect_b64 s[6:7], -1, 0
	s_and_b64 s[0:1], s[6:7], s[2:3]
	s_andn2_b64 vcc, exec, s[0:1]
	v_writelane_b32 v254, s60, 4
	s_cbranch_vccnz .LBB0_260
	s_mov_b64 s[2:3], s[80:81]
	s_load_dwordx2 s[8:9], s[2:3], 0xa8
	s_cmpk_lg_i32 s56, 0x100
	s_cselect_b32 s0, s56, 0xb4
	s_cmp_ge_i32 s78, s0
	s_mov_b64 s[4:5], -1
	s_cbranch_scc0 .LBB0_145
	s_sub_i32 s1, s78, s0
	s_cmpk_gt_i32 s1, 0x2567
	s_cbranch_scc1 .LBB0_144
	s_sub_i32 s20, s56, s0
	s_abs_i32 s4, s20
	v_cvt_f32_u32_e32 v1, s4
	s_load_dwordx2 s[10:11], s[2:3], 0x78
	s_load_dwordx2 s[12:13], s[2:3], 0x88
	s_sub_i32 s2, s20, s1
	s_add_i32 s3, s2, 0x2567
	v_rcp_iflag_f32_e32 v1, v1
	s_sub_i32 s2, 0xffffda99, s2
	s_xor_b32 s14, s3, s20
	s_sub_i32 s5, 0, s4
	v_mul_f32_e32 v1, 0x4f7ffffe, v1
	v_cvt_u32_f32_e32 v1, v1
	s_max_i32 s2, s3, s2
	s_ashr_i32 s3, s14, 31
	v_readfirstlane_b32 s14, v1
	s_mul_i32 s5, s5, s14
	s_mul_hi_u32 s5, s14, s5
	s_add_i32 s14, s14, s5
	s_mul_hi_u32 s5, s2, s14
	s_mul_i32 s14, s5, s4
	s_sub_i32 s2, s2, s14
	s_add_i32 s14, s5, 1
	s_sub_i32 s15, s2, s4
	s_cmp_ge_u32 s2, s4
	s_cselect_b32 s5, s14, s5
	s_cselect_b32 s2, s15, s2
	s_add_i32 s14, s5, 1
	s_cmp_ge_u32 s2, s4
	s_cselect_b32 s2, s14, s5
	s_xor_b32 s2, s2, s3
	s_sub_i32 s29, s2, s3
	s_lshl_b32 s21, s29, 2
	s_add_i32 s22, s21, -1
	s_cmp_gt_i32 s29, 0
	s_cselect_b64 s[2:3], -1, 0
	s_and_b64 s[4:5], s[2:3], exec
	s_cselect_b32 s18, 0, s22
	s_ashr_i32 s4, s18, 2
	s_mul_i32 s17, s4, s20
	s_add_i32 s17, s17, s1
	s_cmpk_gt_i32 s17, 0x1fff
	s_mov_b32 s5, 0
	s_cbranch_scc0 .LBB0_91
	s_add_i32 s4, s17, 0xffffe000
	s_lshr_b32 s4, s4, 7
	s_lshl_b64 s[4:5], s[4:5], 24
	s_waitcnt lgkmcnt(0)
	s_add_u32 s14, s12, s4
	s_addc_u32 s15, s13, s5
	s_lshl_b32 s4, s17, 4
	s_and_b32 s26, s4, 0x780
	s_lshl_b32 s4, s17, 8
	s_and_b32 s16, s4, 0x700
	s_mov_b64 s[4:5], 0x800
	s_cbranch_execz .LBB0_92
	s_branch .LBB0_93

.LBB0_367:
	s_lshr_b32 s0, s56, 31
	s_add_i32 s0, s56, s0
	s_ashr_i32 s0, s0, 1
	v_readlane_b32 s78, v254, 5
	s_cmp_ge_i32 s78, s0
	v_readlane_b32 s79, v254, 8
	v_readlane_b32 s60, v254, 4
	s_cbranch_scc0 .LBB0_409
	s_sub_i32 s10, s78, s0
	s_cmpk_gt_u32 s10, 0x37f
	s_waitcnt vmcnt(0) lgkmcnt(0)
	s_barrier
	s_cbranch_scc1 .LBB0_409
	s_sub_i32 s0, s56, s0
	s_abs_i32 s2, s0
	v_cvt_f32_u32_e32 v2, s2
	s_sub_i32 s3, s0, s10
	s_add_i32 s4, s3, 0x37f
	s_sub_i32 s3, 0xfffffc81, s3
	v_rcp_iflag_f32_e32 v2, v2
	s_xor_b32 s6, s4, s0
	s_sub_i32 s5, 0, s2
	s_max_i32 s3, s4, s3
	v_mul_f32_e32 v2, 0x4f7ffffe, v2
	v_cvt_u32_f32_e32 v2, v2
	s_ashr_i32 s4, s6, 31
	s_add_i32 s1, s10, 0x2568
	v_readfirstlane_b32 s6, v2
	s_mul_i32 s5, s5, s6
	s_mul_hi_u32 s5, s6, s5
	s_add_i32 s6, s6, s5
	s_mul_hi_u32 s5, s3, s6
	s_mul_i32 s6, s5, s2
	s_sub_i32 s3, s3, s6
	s_add_i32 s7, s5, 1
	s_sub_i32 s6, s3, s2
	s_cmp_ge_u32 s3, s2
	s_cselect_b32 s5, s7, s5
	s_cselect_b32 s3, s6, s3
	s_add_i32 s6, s5, 1
	s_cmp_ge_u32 s3, s2
	s_cselect_b32 s2, s6, s5
	s_xor_b32 s2, s2, s4
	s_sub_i32 s18, s2, s4
	s_lshl_b32 s12, s18, 2
	s_add_i32 s13, s12, -1
	s_cmp_gt_i32 s18, 0
	s_cselect_b64 s[2:3], -1, 0
	s_and_b64 s[4:5], s[2:3], exec
	s_cselect_b32 s11, 0, s13
	s_ashr_i32 s4, s11, 2
	s_mul_i32 s9, s4, s0
	s_add_i32 s9, s9, s1
	s_cmpk_gt_i32 s9, 0x1fff
	s_mov_b32 s5, 0
	s_cbranch_scc0 .LBB0_371
	s_add_i32 s4, s9, 0xffffe000
	s_lshr_b32 s4, s4, 7
	s_lshl_b64 s[4:5], s[4:5], 24
	v_readlane_b32 s34, v254, 13
	v_readlane_b32 s35, v254, 14
	s_add_u32 s6, s34, s4
	s_addc_u32 s7, s35, s5
	s_lshl_b32 s4, s9, 4
	s_and_b32 s19, s4, 0x780
	s_lshl_b32 s4, s9, 8
	v_readlane_b32 s30, v254, 11
	s_and_b32 s8, s4, 0x700
	v_readlane_b32 s31, v254, 12
	s_mov_b64 s[4:5], 0x800
	s_cbranch_execz .LBB0_372
	s_branch .LBB0_373

.LBB0_387:
	s_max_i32 s9, s12, 1
	s_add_u32 s18, s66, 0x5ee00000
	s_addc_u32 s19, s67, 0
	s_ashr_i32 s7, s6, 31
	s_lshl_b64 s[6:7], s[6:7], 2
	s_add_u32 s4, s4, s6
	v_add_u32_e32 v3, s8, v14
	v_mov_b32_e32 v11, 0
	s_addc_u32 s5, s5, s7
	v_mad_i64_i32 v[12:13], s[6:7], s2, v3, 0
	v_lshl_add_u64 v[12:13], v[12:13], 2, s[4:5]
	v_mov_b32_e32 v3, v11
	v_lshl_add_u64 v[12:13], v[12:13], 0, v[2:3]
	s_mov_b64 s[6:7], 0x300
	s_add_i32 s27, 0, 0x18000
	v_lshl_add_u64 v[12:13], v[12:13], 0, s[6:7]
	s_add_i32 m0, s27, s14
	v_add_u32_e32 v3, s8, v15
	global_load_lds_dwordx4 v[12:13], off nt
	v_mad_i64_i32 v[12:13], s[28:29], s2, v3, 0
	v_lshl_add_u64 v[12:13], v[12:13], 2, s[4:5]
	v_mov_b32_e32 v5, v11
	v_lshl_add_u64 v[12:13], v[12:13], 0, v[4:5]
	v_lshl_add_u64 v[12:13], v[12:13], 0, s[6:7]
	s_add_i32 m0, s27, s15
	v_add_u32_e32 v3, s8, v16
	global_load_lds_dwordx4 v[12:13], off nt
	v_mad_i64_i32 v[12:13], s[28:29], s2, v3, 0
	v_lshl_add_u64 v[12:13], v[12:13], 2, s[4:5]
	v_mov_b32_e32 v7, v11
	v_lshl_add_u64 v[12:13], v[12:13], 0, v[6:7]
	v_lshl_add_u64 v[12:13], v[12:13], 0, s[6:7]
	s_add_i32 m0, s27, s16
	v_add_u32_e32 v3, s8, v1
	global_load_lds_dwordx4 v[12:13], off nt
	v_mad_i64_i32 v[12:13], s[2:3], s2, v3, 0
	v_lshl_add_u64 v[12:13], v[12:13], 2, s[4:5]
	v_mov_b32_e32 v9, v11
	v_lshl_add_u64 v[12:13], v[12:13], 0, v[8:9]
	v_lshl_add_u64 v[12:13], v[12:13], 0, s[6:7]
	s_add_i32 m0, s27, s17
	v_lshrrev_b32_e32 v19, 3, v162
	global_load_lds_dwordx4 v[12:13], off nt
	v_readlane_b32 s2, v254, 15
	v_and_b32_e32 v3, 7, v0
	v_lshrrev_b32_e32 v9, 1, v162
	v_or_b32_e32 v17, s2, v19
	v_lshrrev_b32_e32 v7, 2, v17
	v_bitop3_b32 v7, v7, v0, 7 bitop3:0x78
	v_lshl_add_u32 v5, v3, 12, 0
	v_lshlrev_b32_e32 v7, 4, v7
	v_and_b32_e32 v9, 12, v9
	v_add3_u32 v18, v5, v7, v9
	ds_read2st64_b32 v[12:13], v18 offset1:1
	ds_read2st64_b32 v[20:21], v18 offset0:2 offset1:3
	ds_read2st64_b32 v[22:23], v18 offset0:4 offset1:5
	ds_read2st64_b32 v[24:25], v18 offset0:6 offset1:7
	v_lshlrev_b32_e32 v10, 4, v3
	s_lshl_b32 s2, s10, 15
	s_waitcnt lgkmcnt(0)
	v_mul_f32_e32 v7, 0x42000000, v20
	v_mul_f32_e32 v3, 0x42000000, v12
	v_mul_f32_e32 v5, 0x42000000, v13
	ds_read2st64_b32 v[12:13], v18 offset0:8 offset1:9
	v_mul_f32_e32 v9, 0x42000000, v21
	v_mul_f32_e32 v26, 0x42000000, v22
	v_mul_f32_e32 v27, 0x42000000, v23
	v_mul_f32_e32 v28, 0x42000000, v24
	v_mul_f32_e32 v29, 0x42000000, v25
	ds_read2st64_b32 v[20:21], v18 offset0:10 offset1:11
	ds_read2st64_b32 v[22:23], v18 offset0:12 offset1:13
	ds_read2st64_b32 v[24:25], v18 offset0:14 offset1:15
	s_add_i32 s2, s2, 0x2b40000
	s_and_b32 s2, s2, 0x7c00000
	s_waitcnt lgkmcnt(0)
	v_mul_f32_e32 v30, 0x42000000, v12
	v_mul_f32_e32 v13, 0x42000000, v13
	v_mul_f32_e32 v31, 0x42000000, v20
	v_mul_f32_e32 v32, 0x42000000, v21
	v_mul_f32_e32 v33, 0x42000000, v22
	v_mul_f32_e32 v34, 0x42000000, v23
	v_mov_b32_e32 v20, v11
	v_mov_b32_e32 v21, v11
	v_mov_b32_e32 v22, v11
	v_mov_b32_e32 v23, v11
	s_add_u32 s4, s18, s2
	v_cvt_pk_fp8_f32 v20, v3, v5
	v_cvt_pk_fp8_f32 v21, v26, v27
	v_cvt_pk_fp8_f32 v22, v30, v13
	v_cvt_pk_fp8_f32 v23, v33, v34
	s_addc_u32 s5, s19, 0
	s_lshl_b32 s6, s1, 8
	s_and_b32 s6, s6, 0x700
	v_mul_f32_e32 v3, 0x42000000, v24
	v_mul_f32_e32 v5, 0x42000000, v25
	v_add_u32_e32 v12, s6, v17
	v_mov_b32_e32 v13, v11
	s_lshl_b32 s2, s1, 4
	v_cvt_pk_fp8_f32 v20, v7, v9 op_sel:[0,0,1]
	v_cvt_pk_fp8_f32 v21, v28, v29 op_sel:[0,0,1]
	v_cvt_pk_fp8_f32 v22, v31, v32 op_sel:[0,0,1]
	v_cvt_pk_fp8_f32 v23, v3, v5 op_sel:[0,0,1]
	v_lshlrev_b64 v[24:25], 11, v[12:13]
	s_mov_b32 s3, 0
	s_and_b32 s2, s2, 0x780
	v_lshl_add_u64 v[24:25], s[4:5], 0, v[24:25]
	v_lshl_add_u64 v[24:25], v[24:25], 0, s[2:3]
	v_lshl_add_u64 v[24:25], v[24:25], 0, v[10:11]
	s_cmp_eq_u32 s9, 1
	global_store_dwordx4 v[24:25], v[20:23], off nt
	s_cbranch_scc1 .LBB0_408
	s_min_i32 s27, s13, 4
	s_ashr_i32 s6, s27, 2
	s_waitcnt vmcnt(9)
	s_barrier
	s_mul_i32 s29, s6, s0
	s_add_i32 s29, s29, s1
	s_cmpk_lt_i32 s29, 0x2000
	s_cbranch_scc1 .LBB0_390
	s_add_i32 s6, s29, 0xffffe000
	s_lshr_b32 s6, s6, 7
	s_mov_b32 s7, 0
	s_lshl_b64 s[6:7], s[6:7], 24
	s_add_u32 s8, s34, s6
	s_addc_u32 s9, s35, s7
	s_lshl_b32 s6, s29, 4
	s_and_b32 s28, s6, 0x780
	s_lshl_b32 s6, s29, 8
	s_and_b32 s10, s6, 0x700
	s_mov_b64 s[6:7], 0
	s_branch .LBB0_391

.LBB0_734:
	s_add_u32 s10, s48, 0xc000
	v_lshrrev_b32_e32 v8, 6, v0
	v_and_b32_e32 v2, 0xfc, v1
	s_addc_u32 s11, s49, 0
	v_mul_u32_u24_e32 v1, 0x410, v8
	v_lshlrev_b32_e32 v4, 2, v2
	s_mov_b32 s4, 0x10400
	v_lshrrev_b32_e32 v39, 1, v0
	v_and_b32_e32 v5, 1, v0
	s_add_u32 s22, s16, 0x5ee00000
	v_add3_u32 v1, 0, v1, v4
	v_lshlrev_b32_e32 v4, 6, v5
	v_mad_u32_u24 v5, v5, s4, 0
	v_lshlrev_b32_e32 v7, 2, v39
	v_lshrrev_b32_e32 v6, 2, v0
	s_addc_u32 s23, s17, 0
	v_mov_b32_e32 v3, 0
	v_add3_u32 v40, v5, v4, v7
	v_lshlrev_b32_e32 v7, 7, v39
	s_movk_i32 s4, 0xff
	s_add_i32 s24, 0, 0x27fd0
	s_mov_b32 s5, 0
	v_cmp_eq_u32_e64 s[2:3], 0, v0
	v_or_b32_e32 v9, 8, v8
	v_add_u32_e32 v10, 0x2080, v1
	v_or_b32_e32 v11, 16, v8
	v_add_u32_e32 v12, 0x4100, v1
	v_or_b32_e32 v13, 24, v8
	v_add_u32_e32 v14, 0x6180, v1
	v_or_b32_e32 v15, 32, v8
	v_add_u32_e32 v16, 0x8200, v1
	v_or_b32_e32 v17, 40, v8
	v_add_u32_e32 v18, 0xa280, v1
	v_or_b32_e32 v19, 48, v8
	v_add_u32_e32 v20, 0xc300, v1
	v_or_b32_e32 v21, 56, v8
	v_add_u32_e32 v22, 0xe380, v1
	v_or_b32_e32 v23, 64, v8
	v_add_u32_e32 v24, 0x10400, v1
	v_or_b32_e32 v25, 0x48, v8
	v_add_u32_e32 v26, 0x12480, v1
	v_or_b32_e32 v27, 0x50, v8
	v_add_u32_e32 v28, 0x14500, v1
	v_or_b32_e32 v29, 0x58, v8
	v_add_u32_e32 v30, 0x16580, v1
	v_or_b32_e32 v31, 0x60, v8
	v_add_u32_e32 v32, 0x18600, v1
	v_or_b32_e32 v33, 0x68, v8
	v_add_u32_e32 v34, 0x1a680, v1
	v_or_b32_e32 v35, 0x70, v8
	v_add_u32_e32 v36, 0x1c700, v1
	v_or_b32_e32 v37, 0x78, v8
	v_add_u32_e32 v38, 0x1e7c0, v1
	v_mov_b32_e32 v5, v3
	v_bitop3_b32 v41, v7, s4, v6 bitop3:0xc8
	v_mov_b32_e32 v42, s24
	s_movk_i32 s25, 0x717
	v_lshlrev_b32_e32 v2, 2, v2
	s_branch .LBB0_737

.LBB0_741:
	s_or_b64 exec, exec, s[16:17]
	s_waitcnt lgkmcnt(0)
	s_barrier
	ds_read_b32 v6, v42
	s_mov_b64 s[16:17], -1
	s_waitcnt lgkmcnt(0)
	v_cmp_lt_i32_e32 vcc, s25, v6
	v_readfirstlane_b32 s4, v6
	s_cbranch_vccnz .LBB0_736
	s_add_i32 s18, s4, 0x28e8
	s_cmpk_gt_i32 s4, 0xf717
	s_cbranch_scc0 .LBB0_744
	s_addk_i32 s4, 0x8e8
	s_lshr_b32 s4, s4, 7
	s_lshl_b64 s[16:17], s[4:5], 22
	s_lshl_b64 s[20:21], s[4:5], 24
	s_add_u32 s19, s14, s20
	s_addc_u32 s21, s15, s21
	s_add_u32 s16, s22, s16
	s_addc_u32 s17, s23, s17
	s_lshl_b32 s20, s18, 8
	s_lshl_b32 s4, s18, 4
	s_and_b32 s27, s20, 0x700
	s_and_b32 s26, s4, 0x7f0
	s_and_b32 s4, s4, 0x780
	s_lshl_b32 s20, s27, 2
	s_add_u32 s20, s19, s20
	s_addc_u32 s21, s21, 0
	v_or_b32_e32 v43, s4, v8
	v_lshl_add_u64 v[6:7], s[20:21], 0, v[2:3]
	v_lshlrev_b32_e32 v44, 13, v43
	v_mov_b32_e32 v45, v3
	v_or_b32_e32 v43, s4, v9
	v_lshl_add_u64 v[52:53], v[6:7], 0, v[44:45]
	v_lshlrev_b32_e32 v44, 13, v43
	v_or_b32_e32 v43, s4, v11
	v_lshl_add_u64 v[54:55], v[6:7], 0, v[44:45]
	global_load_dwordx4 v[44:47], v[52:53], off
	global_load_dwordx4 v[48:51], v[54:55], off
	v_lshlrev_b32_e32 v52, 13, v43
	v_mov_b32_e32 v53, v3
	v_or_b32_e32 v43, s4, v13
	v_lshl_add_u64 v[60:61], v[6:7], 0, v[52:53]
	v_lshlrev_b32_e32 v52, 13, v43
	v_or_b32_e32 v43, s4, v15
	v_lshl_add_u64 v[62:63], v[6:7], 0, v[52:53]
	global_load_dwordx4 v[52:55], v[60:61], off
	global_load_dwordx4 v[56:59], v[62:63], off
	v_lshlrev_b32_e32 v60, 13, v43
	v_mov_b32_e32 v61, v3
	v_or_b32_e32 v43, s4, v17
	v_lshl_add_u64 v[68:69], v[6:7], 0, v[60:61]
	v_lshlrev_b32_e32 v60, 13, v43
	v_or_b32_e32 v43, s4, v19
	v_lshl_add_u64 v[70:71], v[6:7], 0, v[60:61]
	global_load_dwordx4 v[60:63], v[68:69], off
	global_load_dwordx4 v[64:67], v[70:71], off
	v_lshlrev_b32_e32 v68, 13, v43
	v_mov_b32_e32 v69, v3
	v_or_b32_e32 v43, s4, v21
	v_lshl_add_u64 v[76:77], v[6:7], 0, v[68:69]
	v_lshlrev_b32_e32 v68, 13, v43
	v_or_b32_e32 v43, s4, v23
	v_lshl_add_u64 v[78:79], v[6:7], 0, v[68:69]
	global_load_dwordx4 v[68:71], v[76:77], off
	global_load_dwordx4 v[72:75], v[78:79], off
	v_lshlrev_b32_e32 v76, 13, v43
	v_mov_b32_e32 v77, v3
	v_or_b32_e32 v43, s4, v25
	v_lshl_add_u64 v[84:85], v[6:7], 0, v[76:77]
	v_lshlrev_b32_e32 v76, 13, v43
	v_or_b32_e32 v43, s4, v27
	v_lshl_add_u64 v[86:87], v[6:7], 0, v[76:77]
	global_load_dwordx4 v[76:79], v[84:85], off
	global_load_dwordx4 v[80:83], v[86:87], off
	v_lshlrev_b32_e32 v84, 13, v43
	v_mov_b32_e32 v85, v3
	v_or_b32_e32 v43, s4, v29
	v_lshl_add_u64 v[92:93], v[6:7], 0, v[84:85]
	v_lshlrev_b32_e32 v84, 13, v43
	v_or_b32_e32 v43, s4, v31
	v_lshl_add_u64 v[94:95], v[6:7], 0, v[84:85]
	global_load_dwordx4 v[84:87], v[92:93], off
	global_load_dwordx4 v[88:91], v[94:95], off
	v_lshlrev_b32_e32 v92, 13, v43
	v_mov_b32_e32 v93, v3
	v_or_b32_e32 v43, s4, v33
	v_lshl_add_u64 v[100:101], v[6:7], 0, v[92:93]
	v_lshlrev_b32_e32 v92, 13, v43
	v_or_b32_e32 v43, s26, v35
	v_lshl_add_u64 v[102:103], v[6:7], 0, v[92:93]
	global_load_dwordx4 v[92:95], v[100:101], off
	global_load_dwordx4 v[96:99], v[102:103], off
	v_lshlrev_b32_e32 v100, 13, v43
	v_mov_b32_e32 v101, v3
	v_or_b32_e32 v43, s4, v37
	v_lshl_add_u64 v[108:109], v[6:7], 0, v[100:101]
	v_lshlrev_b32_e32 v100, 13, v43
	v_lshl_add_u64 v[6:7], v[6:7], 0, v[100:101]
	global_load_dwordx4 v[100:103], v[108:109], off
	global_load_dwordx4 v[104:107], v[6:7], off
	v_or_b32_e32 v6, s27, v39
	v_lshlrev_b32_e32 v6, 11, v6
	v_mov_b32_e32 v7, v3
	v_lshl_add_u64 v[6:7], s[16:17], 0, v[6:7]
	v_lshl_add_u64 v[6:7], v[6:7], 0, s[4:5]
	v_lshl_add_u64 v[6:7], v[6:7], 0, v[4:5]
	s_mov_b64 s[16:17], 0
	s_waitcnt vmcnt(15)
	ds_write_b128 v1, v[44:47]
	s_waitcnt vmcnt(14)
	ds_write_b128 v10, v[48:51]
	s_waitcnt vmcnt(13)
	ds_write_b128 v12, v[52:55]
	s_waitcnt vmcnt(12)
	ds_write_b128 v14, v[56:59]
	s_waitcnt vmcnt(11)
	ds_write_b128 v16, v[60:63]
	s_waitcnt vmcnt(10)
	ds_write_b128 v18, v[64:67]
	s_waitcnt vmcnt(9)
	ds_write_b128 v20, v[68:71]
	s_waitcnt vmcnt(8)
	ds_write_b128 v22, v[72:75]
	s_waitcnt vmcnt(7)
	ds_write_b128 v24, v[76:79] offset:64
	s_waitcnt vmcnt(6)
	ds_write_b128 v26, v[80:83] offset:64
	s_waitcnt vmcnt(5)
	ds_write_b128 v28, v[84:87] offset:64
	s_waitcnt vmcnt(4)
	ds_write_b128 v30, v[88:91] offset:64
	s_waitcnt vmcnt(3)
	ds_write_b128 v32, v[92:95] offset:64
	s_waitcnt vmcnt(2)
	ds_write_b128 v34, v[96:99] offset:64
	s_waitcnt vmcnt(1)
	ds_write_b128 v36, v[100:103] offset:64
	s_waitcnt vmcnt(0)
	ds_write_b128 v38, v[104:107]
	s_waitcnt lgkmcnt(0)
	s_barrier
	ds_read_b32 v43, v40
	ds_read_b32 v44, v40 offset:1040
	ds_read_b32 v45, v40 offset:2080
	ds_read_b32 v46, v40 offset:3120
	ds_read_b32 v47, v40 offset:4160
	ds_read_b32 v48, v40 offset:5200
	ds_read_b32 v49, v40 offset:6240
	ds_read_b32 v50, v40 offset:7280
	s_waitcnt lgkmcnt(6)
	v_mul_f32_e32 v51, 0x42000000, v44
	s_waitcnt lgkmcnt(5)
	v_mul_f32_e32 v52, 0x42000000, v45
	s_waitcnt lgkmcnt(4)
	v_mul_f32_e32 v53, 0x42000000, v46
	s_waitcnt lgkmcnt(3)
	v_mul_f32_e32 v46, 0x42000000, v47
	s_waitcnt lgkmcnt(2)
	v_mul_f32_e32 v47, 0x42000000, v48
	s_waitcnt lgkmcnt(1)
	v_mul_f32_e32 v48, 0x42000000, v49
	s_waitcnt lgkmcnt(0)
	v_mul_f32_e32 v49, 0x42000000, v50
	ds_read_b32 v44, v40 offset:8320
	ds_read_b32 v45, v40 offset:9360
	ds_read_b32 v50, v40 offset:10400
	ds_read_b32 v54, v40 offset:11440
	ds_read_b32 v55, v40 offset:12480
	ds_read_b32 v56, v40 offset:13520
	ds_read_b32 v57, v40 offset:14560
	ds_read_b32 v58, v40 offset:15600
	s_waitcnt lgkmcnt(6)
	v_mul_f32_e32 v60, 0x42000000, v45
	v_mov_b32_e32 v45, v3
	v_mul_f32_e32 v43, 0x42000000, v43
	v_mul_f32_e32 v59, 0x42000000, v44
	v_mov_b32_e32 v44, v3
	v_cvt_pk_fp8_f32 v45, v46, v47
	v_mov_b32_e32 v46, v3
	v_cvt_pk_fp8_f32 v44, v43, v51
	v_cvt_pk_fp8_f32 v46, v59, v60
	s_waitcnt lgkmcnt(5)
	v_mul_f32_e32 v50, 0x42000000, v50
	s_waitcnt lgkmcnt(4)
	v_mul_f32_e32 v54, 0x42000000, v54
	s_waitcnt lgkmcnt(3)
	v_mul_f32_e32 v55, 0x42000000, v55
	s_waitcnt lgkmcnt(2)
	v_mul_f32_e32 v56, 0x42000000, v56
	v_mov_b32_e32 v47, v3
	v_cvt_pk_fp8_f32 v44, v52, v53 op_sel:[0,0,1]
	v_cvt_pk_fp8_f32 v45, v48, v49 op_sel:[0,0,1]
	v_cvt_pk_fp8_f32 v46, v50, v54 op_sel:[0,0,1]
	ds_read_b32 v43, v40 offset:16640
	ds_read_b32 v48, v40 offset:17680
	ds_read_b32 v49, v40 offset:18720
	ds_read_b32 v50, v40 offset:19760
	ds_read_b32 v51, v40 offset:20800
	ds_read_b32 v52, v40 offset:21840
	ds_read_b32 v53, v40 offset:22880
	ds_read_b32 v54, v40 offset:23920
	v_cvt_pk_fp8_f32 v47, v55, v56
	s_waitcnt lgkmcnt(9)
	v_mul_f32_e32 v57, 0x42000000, v57
	s_waitcnt lgkmcnt(8)
	v_mul_f32_e32 v58, 0x42000000, v58
	s_waitcnt lgkmcnt(6)
	v_mul_f32_e32 v55, 0x42000000, v48
	v_cvt_pk_fp8_f32 v47, v57, v58 op_sel:[0,0,1]
	s_waitcnt lgkmcnt(5)
	v_mul_f32_e32 v56, 0x42000000, v49
	s_waitcnt lgkmcnt(4)
	v_mul_f32_e32 v57, 0x42000000, v50
	s_waitcnt lgkmcnt(3)
	v_mul_f32_e32 v50, 0x42000000, v51
	s_waitcnt lgkmcnt(2)
	v_mul_f32_e32 v51, 0x42000000, v52
	s_waitcnt lgkmcnt(1)
	v_mul_f32_e32 v52, 0x42000000, v53
	s_waitcnt lgkmcnt(0)
	v_mul_f32_e32 v53, 0x42000000, v54
	ds_read_b32 v48, v40 offset:24960
	ds_read_b32 v49, v40 offset:26000
	ds_read_b32 v54, v40 offset:27040
	ds_read_b32 v58, v40 offset:28080
	ds_read_b32 v59, v40 offset:29120
	ds_read_b32 v60, v40 offset:30160
	ds_read_b32 v61, v40 offset:31200
	ds_read_b32 v62, v40 offset:32240
	s_waitcnt lgkmcnt(6)
	v_mul_f32_e32 v64, 0x42000000, v49
	v_mov_b32_e32 v49, v3
	v_mul_f32_e32 v43, 0x42000000, v43
	v_mul_f32_e32 v63, 0x42000000, v48
	v_mov_b32_e32 v48, v3
	v_cvt_pk_fp8_f32 v49, v50, v51
	v_mov_b32_e32 v50, v3
	v_cvt_pk_fp8_f32 v48, v43, v55
	v_cvt_pk_fp8_f32 v50, v63, v64
	s_waitcnt lgkmcnt(5)
	v_mul_f32_e32 v54, 0x42000000, v54
	s_waitcnt lgkmcnt(4)
	v_mul_f32_e32 v58, 0x42000000, v58
	s_waitcnt lgkmcnt(3)
	v_mul_f32_e32 v59, 0x42000000, v59
	s_waitcnt lgkmcnt(2)
	v_mul_f32_e32 v60, 0x42000000, v60
	v_mov_b32_e32 v51, v3
	v_cvt_pk_fp8_f32 v48, v56, v57 op_sel:[0,0,1]
	v_cvt_pk_fp8_f32 v49, v52, v53 op_sel:[0,0,1]
	v_cvt_pk_fp8_f32 v50, v54, v58 op_sel:[0,0,1]
	ds_read_b32 v43, v40 offset:33280
	ds_read_b32 v52, v40 offset:34320
	ds_read_b32 v53, v40 offset:35360
	ds_read_b32 v54, v40 offset:36400
	ds_read_b32 v55, v40 offset:37440
	ds_read_b32 v56, v40 offset:38480
	ds_read_b32 v57, v40 offset:39520
	ds_read_b32 v58, v40 offset:40560
	v_cvt_pk_fp8_f32 v51, v59, v60
	s_waitcnt lgkmcnt(9)
	v_mul_f32_e32 v61, 0x42000000, v61
	s_waitcnt lgkmcnt(8)
	v_mul_f32_e32 v62, 0x42000000, v62
	s_waitcnt lgkmcnt(6)
	v_mul_f32_e32 v59, 0x42000000, v52
	v_cvt_pk_fp8_f32 v51, v61, v62 op_sel:[0,0,1]
	s_waitcnt lgkmcnt(5)
	v_mul_f32_e32 v60, 0x42000000, v53
	s_waitcnt lgkmcnt(4)
	v_mul_f32_e32 v61, 0x42000000, v54
	s_waitcnt lgkmcnt(3)
	v_mul_f32_e32 v54, 0x42000000, v55
	s_waitcnt lgkmcnt(2)
	v_mul_f32_e32 v55, 0x42000000, v56
	s_waitcnt lgkmcnt(1)
	v_mul_f32_e32 v56, 0x42000000, v57
	s_waitcnt lgkmcnt(0)
	v_mul_f32_e32 v57, 0x42000000, v58
	ds_read_b32 v52, v40 offset:41600
	ds_read_b32 v53, v40 offset:42640
	ds_read_b32 v58, v40 offset:43680
	ds_read_b32 v62, v40 offset:44720
	ds_read_b32 v63, v40 offset:45760
	ds_read_b32 v64, v40 offset:46800
	ds_read_b32 v65, v40 offset:47840
	ds_read_b32 v66, v40 offset:48880
	s_waitcnt lgkmcnt(6)
	v_mul_f32_e32 v68, 0x42000000, v53
	v_mov_b32_e32 v53, v3
	v_mul_f32_e32 v43, 0x42000000, v43
	v_mul_f32_e32 v67, 0x42000000, v52
	v_mov_b32_e32 v52, v3
	v_cvt_pk_fp8_f32 v53, v54, v55
	v_mov_b32_e32 v54, v3
	v_cvt_pk_fp8_f32 v52, v43, v59
	v_cvt_pk_fp8_f32 v54, v67, v68
	s_waitcnt lgkmcnt(5)
	v_mul_f32_e32 v58, 0x42000000, v58
	s_waitcnt lgkmcnt(4)
	v_mul_f32_e32 v62, 0x42000000, v62
	s_waitcnt lgkmcnt(3)
	v_mul_f32_e32 v63, 0x42000000, v63
	s_waitcnt lgkmcnt(2)
	v_mul_f32_e32 v64, 0x42000000, v64
	v_mov_b32_e32 v55, v3
	v_cvt_pk_fp8_f32 v52, v60, v61 op_sel:[0,0,1]
	v_cvt_pk_fp8_f32 v53, v56, v57 op_sel:[0,0,1]
	v_cvt_pk_fp8_f32 v54, v58, v62 op_sel:[0,0,1]
	ds_read_b32 v43, v40 offset:49920
	ds_read_b32 v56, v40 offset:50960
	ds_read_b32 v57, v40 offset:52000
	ds_read_b32 v58, v40 offset:53040
	ds_read_b32 v59, v40 offset:54080
	ds_read_b32 v60, v40 offset:55120
	ds_read_b32 v61, v40 offset:56160
	ds_read_b32 v62, v40 offset:57200
	v_cvt_pk_fp8_f32 v55, v63, v64
	s_waitcnt lgkmcnt(9)
	v_mul_f32_e32 v65, 0x42000000, v65
	s_waitcnt lgkmcnt(8)
	v_mul_f32_e32 v66, 0x42000000, v66
	s_waitcnt lgkmcnt(6)
	v_mul_f32_e32 v63, 0x42000000, v56
	v_cvt_pk_fp8_f32 v55, v65, v66 op_sel:[0,0,1]
	s_waitcnt lgkmcnt(5)
	v_mul_f32_e32 v64, 0x42000000, v57
	s_waitcnt lgkmcnt(4)
	v_mul_f32_e32 v65, 0x42000000, v58
	s_waitcnt lgkmcnt(3)
	v_mul_f32_e32 v58, 0x42000000, v59
	s_waitcnt lgkmcnt(2)
	v_mul_f32_e32 v59, 0x42000000, v60
	s_waitcnt lgkmcnt(1)
	v_mul_f32_e32 v60, 0x42000000, v61
	s_waitcnt lgkmcnt(0)
	v_mul_f32_e32 v61, 0x42000000, v62
	ds_read_b32 v56, v40 offset:58240
	ds_read_b32 v57, v40 offset:59280
	ds_read_b32 v62, v40 offset:60320
	ds_read_b32 v66, v40 offset:61360
	ds_read_b32 v67, v40 offset:62400
	ds_read_b32 v68, v40 offset:63440
	ds_read_b32 v69, v40 offset:64480
	ds_read_b32 v70, v40 offset:65520
	s_waitcnt lgkmcnt(6)
	v_mul_f32_e32 v72, 0x42000000, v57
	v_mov_b32_e32 v57, v3
	v_mul_f32_e32 v43, 0x42000000, v43
	v_mul_f32_e32 v71, 0x42000000, v56
	s_waitcnt lgkmcnt(3)
	v_mul_f32_e32 v67, 0x42000000, v67
	s_waitcnt lgkmcnt(2)
	v_mul_f32_e32 v68, 0x42000000, v68
	v_mov_b32_e32 v56, v3
	v_cvt_pk_fp8_f32 v57, v58, v59
	v_mov_b32_e32 v58, v3
	v_mov_b32_e32 v59, v3
	v_cvt_pk_fp8_f32 v56, v43, v63
	v_cvt_pk_fp8_f32 v58, v71, v72
	v_cvt_pk_fp8_f32 v59, v67, v68
	v_mul_f32_e32 v62, 0x42000000, v62
	v_mul_f32_e32 v66, 0x42000000, v66
	s_waitcnt lgkmcnt(1)
	v_mul_f32_e32 v69, 0x42000000, v69
	s_waitcnt lgkmcnt(0)
	v_mul_f32_e32 v70, 0x42000000, v70
	v_cvt_pk_fp8_f32 v56, v64, v65 op_sel:[0,0,1]
	v_cvt_pk_fp8_f32 v57, v60, v61 op_sel:[0,0,1]
	v_cvt_pk_fp8_f32 v58, v62, v66 op_sel:[0,0,1]
	v_cvt_pk_fp8_f32 v59, v69, v70 op_sel:[0,0,1]
	global_store_dwordx4 v[6:7], v[44:47], off
	global_store_dwordx4 v[6:7], v[48:51], off offset:16
	global_store_dwordx4 v[6:7], v[52:55], off offset:32
	global_store_dwordx4 v[6:7], v[56:59], off offset:48
	s_waitcnt lgkmcnt(0)
	s_barrier
